# s15
# baseline (speedup 1.0000x reference)
_Z11attn_kernelILi4EEvPKfS1_S1_S1_S1_S1_PKcPf:
	s_load_dwordx2 s[24:25], s[0:1], 0x30
	s_load_dwordx8 s[8:15], s[0:1], 0x0
	s_load_dwordx4 s[16:19], s[0:1], 0x20
	v_lshrrev_b32_e32 v63, 6, v0
	v_and_b32_e32 v57, 15, v0
	v_bfe_u32 v1, v0, 4, 2
	v_lshrrev_b32_e32 v2, 2, v57
	v_mul_u32_u24_e32 v4, 3, v1
	v_mul_u32_u24_e32 v2, 3, v2
	v_mad_u32_u24 v4, v63, 12, v4
	v_mad_u32_u24 v2, v63, 12, v2
	v_lshlrev_b32_e32 v4, 2, v4
	v_lshlrev_b32_e32 v2, 2, v2
	v_and_b32_e32 v104, 63, v0
	v_lshlrev_b32_e32 v60, 5, v57
	v_lshlrev_b32_e32 v58, 3, v1
	v_add_u32_e32 v3, v60, v58
	v_lshrrev_b32_e32 v56, 4, v0
	v_lshlrev_b32_e32 v54, 4, v57
	v_mov_b32_e32 v59, 0
	s_movk_i32 s4, 0xe0
	v_cmp_gt_u32_e64 s[4:5], s4, v0
	s_lshl_b32 s26, s2, 8
	s_lshl_b32 s27, s2, 9
	s_mul_i32 s28, s2, 14
	s_add_u32 s26, s26, 0x164000
	s_add_u32 s27, s27, 0x80000
	s_add_u32 s20, s26, 0xc0
	v_min_u32_e32 v5, 2, v57
	v_lshlrev_b32_e32 v147, 6, v57
	v_lshlrev_b32_e32 v5, 2, v5
	v_add_u32_e32 v2, s26, v2
	v_add_u32_e32 v4, s26, v4
	v_add_u32_e32 v3, s27, v3
	v_mul_u32_u24_e32 v156, 0x140, v1
	s_movk_i32 s21, 0x500
	v_mad_u32_u24 v156, v63, s21, v156
	v_lshl_or_b32 v156, v57, 2, v156
	v_add_u32_e32 v156, 0x1c00, v156
	v_lshlrev_b32_e32 v157, 5, v56
	v_cmp_gt_u32_e32 vcc, 3, v57
	v_add_u32_e32 v158, 4, v57
	v_lshlrev_b32_e32 v159, 2, v57
	s_movk_i32 s21, 0x50
	v_cndmask_b32_e32 v158, 4, v158, vcc
	v_mad_u32_u24 v159, v56, s21, v159
	v_lshl_add_u32 v158, v158, 2, v157
	v_mul_u32_u24_e32 v250, 0x50, v56
	v_or_b32_e32 v250, 0x3800, v250
	v_lshl_add_u32 v251, v57, 1, v250
	v_mul_u32_u24_e32 v252, 0x50, v57
	v_lshl_add_u32 v252, v58, 1, v252
	v_lshlrev_b32_e32 v253, 2, v57
	v_and_b32_e32 v254, 0xc0, v0
	v_lshlrev_b32_e32 v255, 11, v1
	v_or3_b32 v253, v253, v254, v255
	v_add_u32_e32 v254, s28, v56
	v_lshl_add_u32 v254, v254, 9, v54
	v_lshl_or_b32 v255, v56, 9, v54
	s_waitcnt lgkmcnt(0)
	global_load_dwordx3 v[80:82], v2, s[24:25]
	global_load_dwordx3 v[84:86], v4, s[24:25]
	global_load_dwordx2 v[64:65], v3, s[24:25]
	s_load_dword s3, s[24:25], s20
	s_add_u32 s22, s24, 0x160000
	s_addc_u32 s23, s25, 0
	v_cndmask_b32_e64 v62, 13, v56, s[4:5]
	v_add_u32_e32 v3, s28, v62
	v_mad_u32_u24 v144, v3, 12, v5
	v_mad_u32_u24 v145, v3, 36, v5
	v_lshl_or_b32 v147, v63, 10, v147
	v_lshl_or_b32 v147, v1, 4, v147
	v_or_b32_e32 v148, 0x1000, v147
	v_lshlrev_b32_e32 v149, 4, v104
	v_lshlrev_b32_e32 v150, 9, v3
	v_add_u32_e32 v150, v150, v54
	v_and_b32_e32 v87, 3, v57
	v_lshlrev_b32_e32 v87, 4, v87
	v_lshl_or_b32 v87, v1, 6, v87
	v_lshlrev_b32_e32 v88, 3, v57
	s_add_u32 s26, s24, 0x100000
	s_addc_u32 s27, s25, 0
	s_add_u32 s28, s24, 0x140000
	s_addc_u32 s29, s25, 0
	s_waitcnt lgkmcnt(0)
	s_bitcmp0_b32 s3, 1
	s_cselect_b64 s[20:21], -1, 0
	s_cbranch_scc1 .LBB1_16
	s_waitcnt vmcnt(1)
	v_lshl_add_u32 v72, v80, 9, v87
	v_lshl_add_u32 v73, v81, 9, v87
	v_lshl_add_u32 v74, v82, 9, v87
	global_load_dwordx4 v[50:53], v72, s[24:25]
	global_load_dwordx4 v[46:49], v72, s[24:25] offset:256
	global_load_dwordx4 v[14:17], v73, s[24:25]
	global_load_dwordx4 v[10:13], v73, s[24:25] offset:256
	global_load_dwordx4 v[6:9], v74, s[24:25]
	global_load_dwordx4 v[2:5], v74, s[24:25] offset:256
	v_lshl_add_u32 v75, v84, 8, v54
	v_lshl_add_u32 v78, v84, 7, v88
	v_lshl_add_u32 v76, v85, 8, v54
	v_lshl_add_u32 v79, v85, 7, v88
	v_lshl_add_u32 v77, v86, 8, v54
	v_lshl_add_u32 v80, v86, 7, v88
	global_load_dwordx4 v[30:33], v75, s[26:27]
	global_load_dwordx2 v[70:71], v78, s[28:29]
	global_load_dwordx4 v[26:29], v76, s[26:27]
	global_load_dwordx2 v[66:67], v79, s[28:29]
	global_load_dwordx4 v[18:21], v77, s[26:27]
	global_load_dwordx2 v[68:69], v80, s[28:29]
	global_load_dword v120, v144, s[12:13]
	global_load_dword v151, v144, s[14:15]
	global_load_dword v97, v145, s[10:11]
	global_load_dword v99, v145, s[10:11] offset:12
	global_load_dword v113, v145, s[10:11] offset:24
	global_load_dwordx4 v[124:127], v147, s[22:23]
	global_load_dwordx4 v[128:131], v148, s[22:23]
	s_mov_b32 exec_hi, 0
	global_load_dwordx4 v[132:135], v149, s[16:17]
	s_mov_b32 exec_hi, -1
	s_mov_b32 exec_lo, 0
	global_load_dwordx4 v[132:135], v149, s[18:19] offset:-512
	s_mov_b32 exec_lo, -1
	global_load_dwordx4 v[136:139], v150, s[8:9]
	global_load_dwordx4 v[140:143], v150, s[8:9] offset:256
	v_mad_u32_u24 v144, v56, 3, v57
	v_add_u32_e32 v145, 56, v144
	v_mul_u32_u24_e32 v146, 0x2493, v144
	v_mul_u32_u24_e32 v147, 0x2493, v145
	v_lshrrev_b32_e32 v146, 16, v146
	v_lshrrev_b32_e32 v147, 16, v147
	v_mul_u32_u24_e32 v146, 66, v146
	v_mul_u32_u24_e32 v147, 66, v147
	v_lshl_add_u32 v144, v144, 1, v146
	v_lshl_add_u32 v145, v145, 1, v147
	v_cmp_lt_u32_e32 vcc, 6, v56
	v_lshlrev_b32_e32 v146, 1, v56
	v_mov_b32_e32 v147, 0x42
	v_cndmask_b32_e32 v147, 0, v147, vcc
	v_add_u32_e32 v146, v146, v147
	s_movk_i32 s6, 0x140
	v_cmp_gt_u32_e32 vcc, s6, v0
	v_lshlrev_b32_e32 v22, 2, v0
	v_mov_b32_e32 v23, 0
	s_and_saveexec_b64 s[6:7], vcc
	ds_write_b32 v22, v23 offset:14336
	s_or_b64 exec, exec, s[6:7]
	v_cmp_gt_u32_e32 vcc, 64, v0
	s_and_saveexec_b64 s[6:7], vcc
	ds_write_b32 v22, v23 offset:15360
	s_or_b64 exec, exec, s[6:7]
	v_bfe_u32 v22, s3, v57, 1
	v_cmp_eq_u32_e32 vcc, 0, v22
	v_mov_b32_e32 v45, 0xc9c35000
	s_mov_b32 s30, 0x3db8aa3b
	s_mov_b32 s31, 0x3db8aa3b
	v_cndmask_b32_e64 v55, 1.0, 0, vcc
	v_mov_b32_e32 v121, 0x3fb8aa3b
	s_bitcmp0_b32 s3, 0
	s_cselect_b64 vcc, -1, 0
	v_cndmask_b32_e32 v34, 0, v45, vcc
	s_bitcmp0_b32 s3, 2
	s_cselect_b64 vcc, -1, 0
	v_cndmask_b32_e32 v36, 0, v45, vcc
	s_bitcmp0_b32 s3, 3
	s_cselect_b64 vcc, -1, 0
	v_cndmask_b32_e32 v37, 0, v45, vcc
	s_bitcmp0_b32 s3, 4
	s_cselect_b64 vcc, -1, 0
	v_cndmask_b32_e32 v22, 0, v45, vcc
	s_bitcmp0_b32 s3, 5
	s_cselect_b64 vcc, -1, 0
	v_cndmask_b32_e32 v23, 0, v45, vcc
	s_bitcmp0_b32 s3, 6
	s_cselect_b64 vcc, -1, 0
	v_cndmask_b32_e32 v24, 0, v45, vcc
	s_bitcmp0_b32 s3, 7
	s_cselect_b64 vcc, -1, 0
	v_cndmask_b32_e32 v25, 0, v45, vcc
	s_bitcmp0_b32 s3, 8
	s_cselect_b64 vcc, -1, 0
	v_cndmask_b32_e32 v38, 0, v45, vcc
	s_bitcmp0_b32 s3, 9
	s_cselect_b64 vcc, -1, 0
	v_cndmask_b32_e32 v39, 0, v45, vcc
	s_bitcmp0_b32 s3, 10
	s_cselect_b64 vcc, -1, 0
	v_cndmask_b32_e32 v40, 0, v45, vcc
	s_bitcmp0_b32 s3, 11
	s_cselect_b64 vcc, -1, 0
	v_cndmask_b32_e32 v41, 0, v45, vcc
	s_bitcmp0_b32 s3, 12
	s_cselect_b64 vcc, -1, 0
	v_cndmask_b32_e32 v42, 0, v45, vcc
	s_bitcmp0_b32 s3, 13
	s_cselect_b64 vcc, -1, 0
	v_cndmask_b32_e32 v43, 0, v45, vcc
	v_mov_b32_e32 v35, 0
	v_mov_b32_e32 v44, v45
	v_mov_b32_e32 v75, 0
	v_mov_b32_e32 v79, 0
	v_mov_b32_e32 v83, 0
	s_waitcnt vmcnt(22)
	v_mfma_f32_16x16x32_fp8_fp8 v[160:163], v[50:51], v[64:65], v[34:37]
	v_mfma_f32_16x16x32_fp8_fp8 v[164:167], v[52:53], v[64:65], v[22:25]
	s_waitcnt vmcnt(21)
	v_mfma_f32_16x16x32_fp8_fp8 v[168:171], v[46:47], v[64:65], v[38:41]
	v_mfma_f32_16x16x32_fp8_fp8 v[172:175], v[48:49], v[64:65], v[42:45]
	s_nop 3
	v_max3_f32 v86, v160, v161, v162
	v_max3_f32 v87, v163, v164, v165
	v_max3_f32 v88, v166, v167, v168
	v_max3_f32 v89, v169, v170, v171
	v_max3_f32 v86, v86, v172, v173
	v_max3_f32 v87, v87, v88, v89
	v_max_f32_e32 v96, v86, v87
	v_mul_f32_e32 v98, 0xbdb8aa3b, v96
	v_pk_fma_f32 v[208:209], v[160:161], s[30:31], v[98:99] op_sel_hi:[1,1,0]
	v_pk_fma_f32 v[210:211], v[162:163], s[30:31], v[98:99] op_sel_hi:[1,1,0]
	v_pk_fma_f32 v[212:213], v[164:165], s[30:31], v[98:99] op_sel_hi:[1,1,0]
	v_pk_fma_f32 v[214:215], v[166:167], s[30:31], v[98:99] op_sel_hi:[1,1,0]
	v_pk_fma_f32 v[216:217], v[168:169], s[30:31], v[98:99] op_sel_hi:[1,1,0]
	v_pk_fma_f32 v[218:219], v[170:171], s[30:31], v[98:99] op_sel_hi:[1,1,0]
	v_pk_fma_f32 v[220:221], v[172:173], s[30:31], v[98:99] op_sel_hi:[1,1,0]
	v_exp_f32_e32 v208, v208
	v_exp_f32_e32 v209, v209
	v_exp_f32_e32 v210, v210
	v_exp_f32_e32 v211, v211
	v_exp_f32_e32 v212, v212
	v_exp_f32_e32 v213, v213
	v_exp_f32_e32 v214, v214
	v_exp_f32_e32 v215, v215
	v_exp_f32_e32 v216, v216
	v_exp_f32_e32 v217, v217
	v_exp_f32_e32 v218, v218
	v_exp_f32_e32 v219, v219
	v_exp_f32_e32 v220, v220
	v_exp_f32_e32 v221, v221
	s_waitcnt vmcnt(20)
	v_mfma_f32_16x16x32_fp8_fp8 v[176:179], v[14:15], v[64:65], v[34:37]
	v_mfma_f32_16x16x32_fp8_fp8 v[180:183], v[16:17], v[64:65], v[22:25]
	s_waitcnt vmcnt(19)
	v_mfma_f32_16x16x32_fp8_fp8 v[184:187], v[10:11], v[64:65], v[38:41]
	v_mfma_f32_16x16x32_fp8_fp8 v[188:191], v[12:13], v[64:65], v[42:45]
	v_pk_add_f32 v[86:87], v[208:209], v[210:211]
	v_pk_add_f32 v[88:89], v[212:213], v[214:215]
	v_pk_add_f32 v[90:91], v[216:217], v[218:219]
	v_pk_mul_f32 v[92:93], v[208:209], v[160:161]
	v_pk_mul_f32 v[94:95], v[210:211], v[162:163]
	v_pk_add_f32 v[86:87], v[86:87], v[220:221]
	v_pk_add_f32 v[88:89], v[88:89], v[90:91]
	v_pk_fma_f32 v[92:93], v[212:213], v[164:165], v[92:93]
	v_pk_fma_f32 v[94:95], v[214:215], v[166:167], v[94:95]
	v_pk_add_f32 v[86:87], v[86:87], v[88:89]
	v_pk_fma_f32 v[92:93], v[216:217], v[168:169], v[92:93]
	v_pk_fma_f32 v[94:95], v[218:219], v[170:171], v[94:95]
	v_add_f32_e32 v86, v86, v87
	v_pk_fma_f32 v[92:93], v[220:221], v[172:173], v[92:93]
	v_rcp_f32_e32 v87, v86
	v_pk_add_f32 v[92:93], v[92:93], v[94:95]
	v_mul_f32_e32 v87, v55, v87
	v_add_f32_e32 v92, v92, v93
	v_mul_f32_e32 v107, v86, v87
	v_mul_f32_e32 v92, v92, v87
	v_mul_f32_e32 v100, 0x43800000, v87
	v_mul_f32_e32 v103, 0x3d800000, v92
	v_max3_f32 v86, v176, v177, v178
	v_max3_f32 v87, v179, v180, v181
	v_max3_f32 v88, v182, v183, v184
	v_max3_f32 v89, v185, v186, v187
	v_max3_f32 v86, v86, v188, v189
	v_max3_f32 v87, v87, v88, v89
	v_max_f32_e32 v96, v86, v87
	v_mul_f32_e32 v98, 0xbdb8aa3b, v96
	v_pk_fma_f32 v[222:223], v[176:177], s[30:31], v[98:99] op_sel_hi:[1,1,0]
	v_pk_fma_f32 v[224:225], v[178:179], s[30:31], v[98:99] op_sel_hi:[1,1,0]
	v_pk_fma_f32 v[226:227], v[180:181], s[30:31], v[98:99] op_sel_hi:[1,1,0]
	v_pk_fma_f32 v[228:229], v[182:183], s[30:31], v[98:99] op_sel_hi:[1,1,0]
	v_pk_fma_f32 v[230:231], v[184:185], s[30:31], v[98:99] op_sel_hi:[1,1,0]
	v_pk_fma_f32 v[232:233], v[186:187], s[30:31], v[98:99] op_sel_hi:[1,1,0]
	v_pk_fma_f32 v[234:235], v[188:189], s[30:31], v[98:99] op_sel_hi:[1,1,0]
	v_exp_f32_e32 v222, v222
	v_exp_f32_e32 v223, v223
	v_exp_f32_e32 v224, v224
	v_exp_f32_e32 v225, v225
	v_exp_f32_e32 v226, v226
	v_exp_f32_e32 v227, v227
	v_exp_f32_e32 v228, v228
	v_exp_f32_e32 v229, v229
	v_exp_f32_e32 v230, v230
	v_exp_f32_e32 v231, v231
	v_exp_f32_e32 v232, v232
	v_exp_f32_e32 v233, v233
	v_exp_f32_e32 v234, v234
	v_exp_f32_e32 v235, v235
	s_waitcnt vmcnt(18)
	v_mfma_f32_16x16x32_fp8_fp8 v[192:195], v[6:7], v[64:65], v[34:37]
	v_mfma_f32_16x16x32_fp8_fp8 v[196:199], v[8:9], v[64:65], v[22:25]
	s_waitcnt vmcnt(17)
	v_mfma_f32_16x16x32_fp8_fp8 v[200:203], v[2:3], v[64:65], v[38:41]
	v_mfma_f32_16x16x32_fp8_fp8 v[204:207], v[4:5], v[64:65], v[42:45]
	v_pk_add_f32 v[86:87], v[222:223], v[224:225]
	v_pk_add_f32 v[88:89], v[226:227], v[228:229]
	v_pk_add_f32 v[90:91], v[230:231], v[232:233]
	v_pk_mul_f32 v[92:93], v[222:223], v[176:177]
	v_pk_mul_f32 v[94:95], v[224:225], v[178:179]
	v_pk_add_f32 v[86:87], v[86:87], v[234:235]
	v_pk_add_f32 v[88:89], v[88:89], v[90:91]
	v_pk_fma_f32 v[92:93], v[226:227], v[180:181], v[92:93]
	v_pk_fma_f32 v[94:95], v[228:229], v[182:183], v[94:95]
	v_pk_add_f32 v[86:87], v[86:87], v[88:89]
	v_pk_fma_f32 v[92:93], v[230:231], v[184:185], v[92:93]
	v_pk_fma_f32 v[94:95], v[232:233], v[186:187], v[94:95]
	v_add_f32_e32 v86, v86, v87
	v_pk_fma_f32 v[92:93], v[234:235], v[188:189], v[92:93]
	v_rcp_f32_e32 v87, v86
	v_pk_add_f32 v[92:93], v[92:93], v[94:95]
	v_mul_f32_e32 v87, v55, v87
	v_add_f32_e32 v92, v92, v93
	v_mul_f32_e32 v108, v86, v87
	v_mul_f32_e32 v92, v92, v87
	v_mul_f32_e32 v101, 0x43800000, v87
	v_mul_f32_e32 v105, 0x3d800000, v92
	v_max3_f32 v86, v192, v193, v194
	v_max3_f32 v87, v195, v196, v197
	v_max3_f32 v88, v198, v199, v200
	v_max3_f32 v89, v201, v202, v203
	v_max3_f32 v86, v86, v204, v205
	v_max3_f32 v87, v87, v88, v89
	v_max_f32_e32 v96, v86, v87
	v_mul_f32_e32 v98, 0xbdb8aa3b, v96
	v_pk_fma_f32 v[236:237], v[192:193], s[30:31], v[98:99] op_sel_hi:[1,1,0]
	v_pk_fma_f32 v[238:239], v[194:195], s[30:31], v[98:99] op_sel_hi:[1,1,0]
	v_pk_fma_f32 v[240:241], v[196:197], s[30:31], v[98:99] op_sel_hi:[1,1,0]
	v_pk_fma_f32 v[242:243], v[198:199], s[30:31], v[98:99] op_sel_hi:[1,1,0]
	v_pk_fma_f32 v[244:245], v[200:201], s[30:31], v[98:99] op_sel_hi:[1,1,0]
	v_pk_fma_f32 v[246:247], v[202:203], s[30:31], v[98:99] op_sel_hi:[1,1,0]
	v_pk_fma_f32 v[248:249], v[204:205], s[30:31], v[98:99] op_sel_hi:[1,1,0]
	v_exp_f32_e32 v236, v236
	v_exp_f32_e32 v237, v237
	v_exp_f32_e32 v238, v238
	v_exp_f32_e32 v239, v239
	v_exp_f32_e32 v240, v240
	v_exp_f32_e32 v241, v241
	v_exp_f32_e32 v242, v242
	v_exp_f32_e32 v243, v243
	v_exp_f32_e32 v244, v244
	v_exp_f32_e32 v245, v245
	v_exp_f32_e32 v246, v246
	v_exp_f32_e32 v247, v247
	v_exp_f32_e32 v248, v248
	v_exp_f32_e32 v249, v249
	v_pk_add_f32 v[86:87], v[236:237], v[238:239]
	v_pk_add_f32 v[88:89], v[240:241], v[242:243]
	v_pk_add_f32 v[90:91], v[244:245], v[246:247]
	v_pk_mul_f32 v[92:93], v[236:237], v[192:193]
	v_pk_mul_f32 v[94:95], v[238:239], v[194:195]
	v_pk_add_f32 v[86:87], v[86:87], v[248:249]
	v_pk_add_f32 v[88:89], v[88:89], v[90:91]
	v_pk_fma_f32 v[92:93], v[240:241], v[196:197], v[92:93]
	v_pk_fma_f32 v[94:95], v[242:243], v[198:199], v[94:95]
	v_pk_add_f32 v[86:87], v[86:87], v[88:89]
	v_pk_fma_f32 v[92:93], v[244:245], v[200:201], v[92:93]
	v_pk_fma_f32 v[94:95], v[246:247], v[202:203], v[94:95]
	v_add_f32_e32 v86, v86, v87
	v_pk_fma_f32 v[92:93], v[248:249], v[204:205], v[92:93]
	v_rcp_f32_e32 v87, v86
	v_pk_add_f32 v[92:93], v[92:93], v[94:95]
	v_mul_f32_e32 v87, v55, v87
	v_add_f32_e32 v92, v92, v93
	v_mul_f32_e32 v109, v86, v87
	v_mul_f32_e32 v92, v92, v87
	v_mul_f32_e32 v102, 0x43800000, v87
	v_mul_f32_e32 v106, 0x3d800000, v92
	v_max3_f32 v122, v103, v105, v106
	v_cmp_gt_u32_e64 s[6:7], 16, v104
	v_mov_b32_e32 v123, v122
	s_nop 1
	v_permlane16_swap_b32_e32 v122, v123
	v_max_f32_e32 v122, v122, v123
	v_mov_b32_e32 v123, v122
	s_nop 1
	v_permlane32_swap_b32_e32 v122, v123
	v_max_f32_e32 v36, v122, v123
	v_mul_f32_e32 v123, 0x3fb8aa3b, v36
	v_fma_f32 v111, v103, v121, -v123
	v_exp_f32_e32 v111, v111
	s_nop 0
	v_mul_f32_e32 v112, v111, v100
	v_mul_f32_e32 v110, v111, v107
	v_mov_b32_e32 v114, v111
	v_pk_mul_f32 v[208:209], v[208:209], v[112:113] op_sel_hi:[1,0]
	v_pk_mul_f32 v[210:211], v[210:211], v[112:113] op_sel_hi:[1,0]
	v_pk_mul_f32 v[212:213], v[212:213], v[112:113] op_sel_hi:[1,0]
	v_pk_mul_f32 v[214:215], v[214:215], v[112:113] op_sel_hi:[1,0]
	v_pk_mul_f32 v[216:217], v[216:217], v[112:113] op_sel_hi:[1,0]
	v_pk_mul_f32 v[218:219], v[218:219], v[112:113] op_sel_hi:[1,0]
	v_pk_mul_f32 v[220:221], v[220:221], v[112:113] op_sel_hi:[1,0]
	s_waitcnt vmcnt(15)
	v_mov_b32_e32 v115, v110
	v_fma_mix_f32 v116, v110, v70, 0 op_sel_hi:[0,1,0]
	v_fma_mix_f32 v117, v110, v70, 0 op_sel:[0,1,0] op_sel_hi:[0,1,0]
	v_fma_mix_f32 v118, v110, v71, 0 op_sel_hi:[0,1,0]
	v_cvt_pk_fp8_f32 v72, v208, v209
	v_cvt_pk_fp8_f32 v73, v212, v213
	v_cvt_pk_fp8_f32 v74, v216, v217
	v_cvt_pk_fp8_f32 v75, v220, v221
	v_cvt_pk_fp8_f32 v72, v210, v211 op_sel:[0,0,1]
	v_cvt_pk_fp8_f32 v73, v214, v215 op_sel:[0,0,1]
	v_cvt_pk_fp8_f32 v74, v218, v219 op_sel:[0,0,1]
	s_nop 1
	v_mfma_f32_16x16x32_fp8_fp8 v[152:155], v[72:73], v[30:31], 0
	v_mfma_f32_16x16x32_fp8_fp8 v[152:155], v[74:75], v[32:33], v[152:155]
	v_fma_f32 v111, v105, v121, -v123
	v_exp_f32_e32 v111, v111
	s_nop 0
	v_mul_f32_e32 v112, v111, v101
	v_mul_f32_e32 v110, v111, v108
	v_add_f32_e32 v114, v114, v111
	v_pk_mul_f32 v[222:223], v[222:223], v[112:113] op_sel_hi:[1,0]
	v_pk_mul_f32 v[224:225], v[224:225], v[112:113] op_sel_hi:[1,0]
	v_pk_mul_f32 v[226:227], v[226:227], v[112:113] op_sel_hi:[1,0]
	v_pk_mul_f32 v[228:229], v[228:229], v[112:113] op_sel_hi:[1,0]
	v_pk_mul_f32 v[230:231], v[230:231], v[112:113] op_sel_hi:[1,0]
	v_pk_mul_f32 v[232:233], v[232:233], v[112:113] op_sel_hi:[1,0]
	v_pk_mul_f32 v[234:235], v[234:235], v[112:113] op_sel_hi:[1,0]
	s_waitcnt vmcnt(13)
	v_add_f32_e32 v115, v115, v110
	v_fma_mix_f32 v116, v110, v66, v116 op_sel_hi:[0,1,0]
	v_fma_mix_f32 v117, v110, v66, v117 op_sel:[0,1,0] op_sel_hi:[0,1,0]
	v_fma_mix_f32 v118, v110, v67, v118 op_sel_hi:[0,1,0]
	v_cvt_pk_fp8_f32 v76, v222, v223
	v_cvt_pk_fp8_f32 v77, v226, v227
	v_cvt_pk_fp8_f32 v78, v230, v231
	v_cvt_pk_fp8_f32 v79, v234, v235
	v_cvt_pk_fp8_f32 v76, v224, v225 op_sel:[0,0,1]
	v_cvt_pk_fp8_f32 v77, v228, v229 op_sel:[0,0,1]
	v_cvt_pk_fp8_f32 v78, v232, v233 op_sel:[0,0,1]
	s_nop 1
	v_mfma_f32_16x16x32_fp8_fp8 v[152:155], v[76:77], v[26:27], v[152:155]
	v_mfma_f32_16x16x32_fp8_fp8 v[152:155], v[78:79], v[28:29], v[152:155]
	v_fma_f32 v111, v106, v121, -v123
	v_exp_f32_e32 v111, v111
	s_nop 0
	v_mul_f32_e32 v112, v111, v102
	v_mul_f32_e32 v110, v111, v109
	v_add_f32_e32 v114, v114, v111
	v_pk_mul_f32 v[236:237], v[236:237], v[112:113] op_sel_hi:[1,0]
	v_pk_mul_f32 v[238:239], v[238:239], v[112:113] op_sel_hi:[1,0]
	v_pk_mul_f32 v[240:241], v[240:241], v[112:113] op_sel_hi:[1,0]
	v_pk_mul_f32 v[242:243], v[242:243], v[112:113] op_sel_hi:[1,0]
	v_pk_mul_f32 v[244:245], v[244:245], v[112:113] op_sel_hi:[1,0]
	v_pk_mul_f32 v[246:247], v[246:247], v[112:113] op_sel_hi:[1,0]
	v_pk_mul_f32 v[248:249], v[248:249], v[112:113] op_sel_hi:[1,0]
	s_waitcnt vmcnt(11)
	v_add_f32_e32 v115, v115, v110
	v_fma_mix_f32 v116, v110, v68, v116 op_sel_hi:[0,1,0]
	v_fma_mix_f32 v117, v110, v68, v117 op_sel:[0,1,0] op_sel_hi:[0,1,0]
	v_fma_mix_f32 v118, v110, v69, v118 op_sel_hi:[0,1,0]
	v_cvt_pk_fp8_f32 v80, v236, v237
	v_cvt_pk_fp8_f32 v81, v240, v241
	v_cvt_pk_fp8_f32 v82, v244, v245
	v_cvt_pk_fp8_f32 v83, v248, v249
	v_cvt_pk_fp8_f32 v80, v238, v239 op_sel:[0,0,1]
	v_cvt_pk_fp8_f32 v81, v242, v243 op_sel:[0,0,1]
	v_cvt_pk_fp8_f32 v82, v246, v247 op_sel:[0,0,1]
	s_nop 1
	v_mfma_f32_16x16x32_fp8_fp8 v[152:155], v[80:81], v[18:19], v[152:155]
	v_mfma_f32_16x16x32_fp8_fp8 v[152:155], v[82:83], v[20:21], v[152:155]
	v_mov_b32_e32 v86, v114
	v_mov_b32_e32 v87, v115
	v_mov_b32_e32 v88, v116
	v_mov_b32_e32 v89, v117
	v_mov_b32_e32 v90, v118
	v_permlane16_swap_b32_e32 v114, v86
	v_permlane16_swap_b32_e32 v115, v87
	v_permlane16_swap_b32_e32 v116, v88
	v_permlane16_swap_b32_e32 v117, v89
	v_permlane16_swap_b32_e32 v118, v90
	v_add_f32_e32 v114, v114, v86
	v_add_f32_e32 v115, v115, v87
	v_add_f32_e32 v116, v116, v88
	v_add_f32_e32 v117, v117, v89
	v_add_f32_e32 v118, v118, v90
	v_mov_b32_e32 v86, v114
	v_mov_b32_e32 v87, v115
	v_mov_b32_e32 v88, v116
	v_mov_b32_e32 v89, v117
	v_mov_b32_e32 v90, v118
	v_permlane32_swap_b32_e32 v114, v86
	v_permlane32_swap_b32_e32 v115, v87
	v_permlane32_swap_b32_e32 v116, v88
	v_permlane32_swap_b32_e32 v117, v89
	v_permlane32_swap_b32_e32 v118, v90
	v_add_f32_e32 v37, v114, v86
	v_add_f32_e32 v20, v115, v87
	v_add_f32_e32 v18, v116, v88
	v_add_f32_e32 v19, v117, v89
	v_add_f32_e32 v21, v118, v90
	ds_write2_b32 v156, v152, v153 offset0:0 offset1:20
	ds_write2_b32 v156, v154, v155 offset0:40 offset1:60
	s_branch .LBB1_30
.LBB1_16:
	global_load_dword v120, v144, s[12:13]
	global_load_dword v151, v144, s[14:15]
	global_load_dword v97, v145, s[10:11]
	global_load_dword v99, v145, s[10:11] offset:12
	global_load_dword v113, v145, s[10:11] offset:24
	global_load_dwordx4 v[124:127], v147, s[22:23]
	global_load_dwordx4 v[128:131], v148, s[22:23]
	s_mov_b32 exec_hi, 0
	global_load_dwordx4 v[132:135], v149, s[16:17]
	s_mov_b32 exec_hi, -1
	s_mov_b32 exec_lo, 0
	global_load_dwordx4 v[132:135], v149, s[18:19] offset:-512
	s_mov_b32 exec_lo, -1
	global_load_dwordx4 v[136:139], v150, s[8:9]
	global_load_dwordx4 v[140:143], v150, s[8:9] offset:256
	v_mad_u32_u24 v144, v56, 3, v57
	v_add_u32_e32 v145, 56, v144
	v_mul_u32_u24_e32 v146, 0x2493, v144
	v_mul_u32_u24_e32 v147, 0x2493, v145
	v_lshrrev_b32_e32 v146, 16, v146
	v_lshrrev_b32_e32 v147, 16, v147
	v_mul_u32_u24_e32 v146, 66, v146
	v_mul_u32_u24_e32 v147, 66, v147
	v_lshl_add_u32 v144, v144, 1, v146
	v_lshl_add_u32 v145, v145, 1, v147
	v_cmp_lt_u32_e32 vcc, 6, v56
	v_lshlrev_b32_e32 v146, 1, v56
	v_mov_b32_e32 v147, 0x42
	v_cndmask_b32_e32 v147, 0, v147, vcc
	v_add_u32_e32 v146, v146, v147
	s_movk_i32 s6, 0x140
	v_cmp_gt_u32_e32 vcc, s6, v0
	v_lshlrev_b32_e32 v18, 2, v0
	v_mov_b32_e32 v19, 0
	s_and_saveexec_b64 s[6:7], vcc
	ds_write_b32 v18, v19 offset:14336
	s_or_b64 exec, exec, s[6:7]
	v_cmp_gt_u32_e32 vcc, 64, v0
	s_and_saveexec_b64 s[6:7], vcc
	ds_write_b32 v18, v19 offset:15360
	s_or_b64 exec, exec, s[6:7]
	v_mov_b32_e32 v21, 0
	ds_write2_b32 v156, v21, v21 offset1:20
	ds_write2_b32 v156, v21, v21 offset0:40 offset1:60
	v_cmp_gt_u32_e64 s[6:7], 16, v104
	v_mov_b32_e32 v37, 1.0
	v_mov_b32_e32 v20, 0
	v_mov_b32_e32 v19, 0
	v_mov_b32_e32 v18, 0
	v_mov_b32_e32 v36, 0

.LBB1_32:
	s_or_b64 exec, exec, s[8:9]
	s_movk_i32 s6, 0x100
	v_cmp_gt_u32_e64 s[6:7], s6, v0
	s_waitcnt lgkmcnt(0)
	s_barrier
	s_and_saveexec_b64 s[14:15], s[6:7]
	s_cbranch_execz .LBB1_39
	ds_read_b96 v[160:162], v157 offset:12288
	ds_read_b96 v[164:166], v157 offset:12800
	ds_read_b96 v[168:170], v157 offset:13312
	ds_read_b96 v[172:174], v157 offset:13824
	ds_read2st64_b32 v[176:177], v158 offset0:48 offset1:50
	ds_read2st64_b32 v[178:179], v158 offset0:52 offset1:54
	ds_read2st64_b32 v[180:181], v159 offset0:28 offset1:33
	ds_read2st64_b32 v[182:183], v159 offset0:38 offset1:43
	v_cmp_gt_u32_e32 vcc, 3, v57
	v_cndmask_b32_e64 v18, 1.0, 0, s[20:21]
	s_waitcnt lgkmcnt(4)
	v_max_f32_e32 v21, v160, v164
	v_max3_f32 v33, v21, v168, v172
	v_sub_f32_e32 v21, v160, v33
	v_sub_f32_e32 v29, v164, v33
	v_sub_f32_e32 v30, v168, v33
	v_sub_f32_e32 v33, v172, v33
	v_mul_f32_e32 v21, 0x3fb8aa3b, v21
	v_mul_f32_e32 v29, 0x3fb8aa3b, v29
	v_mul_f32_e32 v30, 0x3fb8aa3b, v30
	v_mul_f32_e32 v33, 0x3fb8aa3b, v33
	v_exp_f32_e32 v21, v21
	v_exp_f32_e32 v29, v29
	v_exp_f32_e32 v30, v30
	v_exp_f32_e32 v33, v33
	v_mov_b32_e32 v20, v250
	v_mul_f32_e32 v35, v21, v161
	v_mul_f32_e32 v34, v21, v162
	v_fmac_f32_e32 v35, v29, v165
	v_fmac_f32_e32 v34, v29, v166
	v_fmac_f32_e32 v35, v30, v169
	v_fmac_f32_e32 v34, v30, v170
	v_fmac_f32_e32 v35, v33, v173
	v_fmac_f32_e32 v34, v33, v174
	v_rcp_f32_e32 v35, v35
	s_waitcnt lgkmcnt(0)
	v_mul_f32_e32 v31, v21, v180
	v_mul_f32_e32 v18, v18, v35
	v_fmac_f32_e32 v31, v29, v181
	v_mul_f32_e32 v35, v21, v176
	v_fmac_f32_e32 v31, v30, v182
	v_fmac_f32_e32 v35, v29, v177
	v_fmac_f32_e32 v31, v33, v183
	v_fmac_f32_e32 v35, v30, v178
	v_mul_f32_e32 v31, v31, v18
	v_fmac_f32_e32 v35, v33, v179
	s_mov_b32 s8, 0x3a800000
	v_fma_mixlo_f16 v31, v31, s8, 0
	v_cmp_eq_u32_e64 s[8:9], 7, v57
	s_and_saveexec_b64 s[10:11], s[4:5]
	ds_write_b16 v251, v31
	s_and_b64 exec, exec, s[8:9]
	v_mov_b32_e32 v31, 0x3c00
	ds_write_b16 v20, v31 offset:46
	s_or_b64 exec, exec, s[10:11]
	s_waitcnt vmcnt(6)
	v_fma_f32 v33, v34, v151, -v35
	v_cmp_eq_u32_e64 s[8:9], 0, v57
	v_fma_f32 v32, v18, v33, -v120
	s_and_b64 s[12:13], vcc, s[4:5]
	s_nop 0
	v_mov_b32_dpp v26, v32 quad_perm:[0,0,0,0] row_mask:0xf bank_mask:0xf bound_ctrl:1
	v_mov_b32_dpp v27, v32 quad_perm:[1,1,1,1] row_mask:0xf bank_mask:0xf bound_ctrl:1
	v_mov_b32_dpp v28, v32 quad_perm:[2,2,2,2] row_mask:0xf bank_mask:0xf bound_ctrl:1
	s_and_b64 exec, exec, s[12:13]
	s_cbranch_execz .LBB1_39
	v_mul_f32_e32 v20, v97, v26
	v_fmac_f32_e32 v20, v99, v27
	v_fmac_f32_e32 v20, v113, v28
	v_mul_f32_e32 v30, v20, v20
	v_cvt_f16_f32_e32 v27, v20
	s_nop 0
	v_mov_b32_dpp v31, v30 quad_perm:[1,2,0,3] row_mask:0xf bank_mask:0xf bound_ctrl:1
	v_mov_b32_dpp v19, v30 quad_perm:[2,0,1,3] row_mask:0xf bank_mask:0xf bound_ctrl:1
	ds_write_b16 v144, v27 offset:14368
	v_add_f32_e32 v18, v30, v31
	v_add_f32_e32 v18, v18, v19
	v_sqrt_f32_e32 v18, v18
	s_nop 0
	v_add_f32_e32 v21, 0x38d1b717, v18
	v_rcp_f32_e32 v21, v21
	s_nop 0
	v_fma_mixlo_f16 v20, v20, v21, 0
	ds_write_b16 v145, v20 offset:14368
	s_and_b64 exec, exec, s[8:9]
	s_cbranch_execz .LBB1_39
	v_cvt_f16_f32_e32 v18, v18
	ds_write_b16 v146, v18 offset:14848
